# v39 + thin2->gate/up GEMM grid barrier replaced by a hand-off among the 32 workgroups of one batch element (global kept for the last mixer)
# baseline (speedup 1.0000x reference)
; __device__ __forceinline__ unsigned xb_ld(unsigned* p)              { return __hip_atomic_load(p, __ATOMIC_RELAXED, __HIP_MEMORY_SCOPE_AGENT); }
; __device__ __forceinline__ unsigned xb_add(unsigned* p, unsigned v) { return __hip_atomic_fetch_add(p, v, __ATOMIC_RELAXED, __HIP_MEMORY_SCOPE_AGENT); }
; #define XB_SPIN(cond, bar) do { unsigned _sp = 0; while (cond) { __builtin_amdgcn_s_sleep(1); \
;     if ((++_sp & 255u) == 0u) { if (xb_ld(&(bar)[XB_TMO])) break; if (_sp > XB_SPIN_CAP) { atomicAdd(&(bar)[XB_TMO], 1u); break; } } } } while (0)
; __device__ __forceinline__ void xcd_barrier(const XcdBarrier& b) {
;     asm volatile("s_waitcnt vmcnt(0)" ::: "memory");
;     __syncthreads();
;     if (threadIdx.x == 0) {
;         unsigned* bar = b.bar;
;         __builtin_amdgcn_s_waitcnt(0);
;         unsigned nloc = b.st[0], nx = b.st[1];
;         if (nloc == 0u) { xcd_barrier_complete(bar, b.x, nloc, nx); b.st[0] = nloc; b.st[1] = nx; }
;         const unsigned old = xb_add(&bar[XB_XSUB(b.x)], 1u);
;         const unsigned gen = old / nloc;
;         if (old + 1u == (gen + 1u) * nloc) {
;             __builtin_amdgcn_fence(__ATOMIC_RELEASE, "agent");
;             asm volatile("s_waitcnt vmcnt(0)" ::: "memory");
;             const unsigned og = xb_add(&bar[XB_TOP], 1u);
;             const unsigned tg = og / nx;
;             if (og + 1u == (tg + 1u) * nx) xb_add(&bar[XB_TOPGEN], 1u);
;             else XB_SPIN(xb_ld(&bar[XB_TOPGEN]) == tg, bar);
;             __builtin_amdgcn_fence(__ATOMIC_ACQUIRE, "agent");
;             xb_add(&bar[XB_XGEN(b.x)], 1u);
;             asm volatile("s_waitcnt vmcnt(0)" ::: "memory");
;         } else {
;             XB_SPIN(xb_ld(&bar[XB_XGEN(b.x)]) == gen, bar);
;             __builtin_amdgcn_fence(__ATOMIC_ACQUIRE, "agent");
;             asm volatile("s_waitcnt vmcnt(0)" ::: "memory");
;         }
;     }
;     __syncthreads();
; }
.LBB0_1759:
	v_readlane_b32 s34, v253, 36
	v_readlane_b32 s35, v253, 37
	s_mov_b32 s0, s76
	s_waitcnt vmcnt(0)
	s_waitcnt lgkmcnt(0)
	s_barrier
	s_mov_b64 s[36:37], exec
	v_readlane_b32 s2, v253, 53
	v_readlane_b32 s3, v253, 54
	s_and_b64 s[2:3], s[36:37], s[2:3]
	s_mov_b64 exec, s[2:3]
	s_cbranch_execz .LBB0_1803
	v_readlane_b32 s14, v253, 55
	s_nop 3
	s_cmp_eq_u32 s14, 6
	s_cbranch_scc1 .Lgh_old_LBB0_1803
	v_readlane_b32 s10, v253, 36
	v_readlane_b32 s11, v253, 37
	v_readlane_b32 s14, v253, 55
	s_nop 3
	s_add_u32 s12, s10, 0xa000
	s_addc_u32 s13, s11, 0
	s_and_b32 s15, s88, 7
	s_lshl_b32 s15, s15, 8
	s_lshr_b32 s14, s14, 1
	s_add_i32 s14, s14, 1
	s_lshl_b32 s14, s14, 5
	v_mov_b32_e32 v2, s15
	v_mov_b32_e32 v5, 1
	global_atomic_add v2, v5, s[12:13]
	s_mov_b32 s18, 0
